# int8 z-projection epilogue: the 8 per-row scales of a unit preloaded before the first block (16 load-wait chains removed)
# speedup vs baseline: 1.0008x; 1.0008x over previous
.LBB0_420:
	s_add_i32 s4, s63, -5
	s_cmp_lt_u32 s4, 4
	v_mov_b32_e32 v130, v142
	v_mov_b32_e32 v149, v143
	s_cselect_b64 s[28:29], -1, 0
	s_lshl_b32 s5, s64, 8
	s_add_i32 s5, s5, s54
	v_add_u32_e32 v130, s5, v130
	v_ashrrev_i32_e32 v131, 31, v130
	v_lshl_add_u64 v[132:133], v[130:131], 2, s[22:23]
	global_load_dword v131, v[132:133], off
	global_load_dword v184, v[132:133], off
	v_add_u32_e32 v192, 16, v130
	v_ashrrev_i32_e32 v193, 31, v192
	v_lshl_add_u64 v[192:193], v[192:193], 2, s[22:23]
	global_load_dword v185, v[192:193], off
	v_add_u32_e32 v194, 32, v130
	v_ashrrev_i32_e32 v195, 31, v194
	v_lshl_add_u64 v[194:195], v[194:195], 2, s[22:23]
	global_load_dword v186, v[194:195], off
	v_add_u32_e32 v192, 48, v130
	v_ashrrev_i32_e32 v193, 31, v192
	v_lshl_add_u64 v[192:193], v[192:193], 2, s[22:23]
	global_load_dword v187, v[192:193], off
	v_add_u32_e32 v194, 128, v130
	v_ashrrev_i32_e32 v195, 31, v194
	v_lshl_add_u64 v[194:195], v[194:195], 2, s[22:23]
	global_load_dword v188, v[194:195], off
	v_add_u32_e32 v192, 144, v130
	v_ashrrev_i32_e32 v193, 31, v192
	v_lshl_add_u64 v[192:193], v[192:193], 2, s[22:23]
	global_load_dword v189, v[192:193], off
	v_add_u32_e32 v194, 160, v130
	v_ashrrev_i32_e32 v195, 31, v194
	v_lshl_add_u64 v[194:195], v[194:195], 2, s[22:23]
	global_load_dword v190, v[194:195], off
	v_add_u32_e32 v192, 176, v130
	v_ashrrev_i32_e32 v193, 31, v192
	v_lshl_add_u64 v[192:193], v[192:193], 2, s[22:23]
	global_load_dword v191, v[192:193], off
	v_cvt_f32_i32_e32 v127, v127
	v_cvt_f32_i32_e32 v126, v126
	v_cvt_f32_i32_e32 v123, v123
	v_cvt_f32_i32_e32 v122, v122
	v_cvt_f32_i32_e32 v135, v129
	v_cvt_f32_i32_e32 v134, v128
	v_cvt_f32_i32_e32 v125, v125
	v_cvt_f32_i32_e32 v124, v124
	s_cmp_gt_u32 s4, 3
	s_waitcnt vmcnt(0)
	v_mul_f32_e32 v136, v141, v131
	v_pk_mul_f32 v[128:129], v[136:137], v[126:127] op_sel_hi:[0,1]
	v_pk_mul_f32 v[126:127], v[136:137], v[122:123] op_sel_hi:[0,1]
	v_pk_mul_f32 v[134:135], v[136:137], v[134:135] op_sel_hi:[0,1]
	v_pk_mul_f32 v[136:137], v[136:137], v[124:125] op_sel_hi:[0,1]
	s_cbranch_scc1 .LBB0_422
	v_mul_f32_e32 v124, 0x3dd2d3e8, v129
	v_fmaak_f32 v124, v129, v124, 0x40135761
	v_mul_f32_e32 v123, 0x3dd2d3e8, v126
	v_mul_f32_e64 v124, v129, -v124
	v_fmaak_f32 v123, v126, v123, 0x40135761
	v_exp_f32_e32 v125, v124
	v_mul_f32_e32 v124, 0x3dd2d3e8, v127
	v_mul_f32_e64 v123, v126, -v123
	v_fmaak_f32 v124, v127, v124, 0x40135761
	v_exp_f32_e32 v123, v123
	v_mul_f32_e64 v124, v127, -v124
	v_exp_f32_e32 v131, v124
	v_mul_f32_e32 v150, 0x3dd2d3e8, v136
	v_add_f32_e32 v123, 1.0, v123
	v_rcp_f32_e32 v124, v123
	v_add_f32_e32 v123, 1.0, v125
	v_add_f32_e32 v125, 1.0, v131
	v_mul_f32_e32 v131, 0x3dd2d3e8, v134
	v_fmaak_f32 v131, v134, v131, 0x40135761
	v_mul_f32_e64 v131, v134, -v131
	v_fmaak_f32 v150, v136, v150, 0x40135761
	v_exp_f32_e32 v131, v131
	v_mul_f32_e64 v150, v136, -v150
	v_exp_f32_e32 v151, v150
	v_mul_f32_e32 v122, 0x3dd2d3e8, v128
	v_add_f32_e32 v131, 1.0, v131
	v_rcp_f32_e32 v150, v131
	v_add_f32_e32 v131, 1.0, v151
	v_mul_f32_e32 v151, 0x3dd2d3e8, v135
	v_fmaak_f32 v151, v135, v151, 0x40135761
	v_mul_f32_e32 v152, 0x3dd2d3e8, v137
	v_fmaak_f32 v122, v128, v122, 0x40135761
	v_mul_f32_e64 v151, v135, -v151
	v_fmaak_f32 v152, v137, v152, 0x40135761
	v_mul_f32_e64 v122, v128, -v122
	v_exp_f32_e32 v151, v151
	v_mul_f32_e64 v152, v137, -v152
	v_exp_f32_e32 v122, v122
	v_exp_f32_e32 v153, v152
	v_rcp_f32_e32 v152, v131
	v_add_f32_e32 v131, 1.0, v151
	v_add_f32_e32 v122, 1.0, v122
	v_rcp_f32_e32 v151, v131
	v_add_f32_e32 v131, 1.0, v153
	v_rcp_f32_e32 v122, v122
	v_rcp_f32_e32 v123, v123
	v_rcp_f32_e32 v125, v125
	v_rcp_f32_e32 v153, v131
	v_pk_mul_f32 v[134:135], v[134:135], v[150:151]
	v_pk_mul_f32 v[128:129], v[128:129], v[122:123]
	v_pk_mul_f32 v[126:127], v[126:127], v[124:125]
	v_pk_mul_f32 v[136:137], v[136:137], v[152:153]
.LBB0_422:
	s_lshl_b32 s10, s63, 8
	v_mov_b64_e32 v[124:125], s[6:7]
	s_ashr_i32 s11, s10, 31
	v_mad_i64_i32 v[124:125], s[4:5], v130, s57, v[124:125]
	v_lshlrev_b32_e32 v122, 3, v149
	v_lshl_add_u64 v[124:125], s[10:11], 1, v[124:125]
	v_ashrrev_i32_e32 v123, 31, v122
	v_lshl_add_u64 v[124:125], v[124:125], 0, s[20:21]
	v_lshl_add_u64 v[124:125], v[122:123], 1, v[124:125]
	v_cvt_pk_bf16_f32 v150, v128, v129
	v_cvt_pk_bf16_f32 v151, v134, v135
	v_cvt_pk_bf16_f32 v152, v126, v127
	v_cvt_pk_bf16_f32 v153, v136, v137
	global_store_dwordx4 v[124:125], v[150:153], off
	v_mov_b32_e32 v126, v184
	v_cvt_f32_i32_e32 v119, v119
	v_cvt_f32_i32_e32 v118, v118
	v_cvt_f32_i32_e32 v115, v115
	v_cvt_f32_i32_e32 v114, v114
	v_cvt_f32_i32_e32 v121, v121
	v_cvt_f32_i32_e32 v120, v120
	v_cvt_f32_i32_e32 v117, v117
	v_cvt_f32_i32_e32 v116, v116
	v_cndmask_b32_e64 v127, 0, 1, s[28:29]
	v_cmp_ne_u32_e64 s[4:5], 1, v127
	s_andn2_b64 vcc, exec, s[28:29]
	v_mul_f32_e32 v126, v141, v126
	v_pk_mul_f32 v[118:119], v[126:127], v[118:119] op_sel_hi:[0,1]
	v_pk_mul_f32 v[114:115], v[126:127], v[114:115] op_sel_hi:[0,1]
	v_pk_mul_f32 v[120:121], v[126:127], v[120:121] op_sel_hi:[0,1]
	v_pk_mul_f32 v[116:117], v[126:127], v[116:117] op_sel_hi:[0,1]
	s_cbranch_vccnz .LBB0_424
	v_mul_f32_e32 v128, 0x3dd2d3e8, v119
	v_fmaak_f32 v128, v119, v128, 0x40135761
	v_mul_f32_e32 v127, 0x3dd2d3e8, v114
	v_mul_f32_e64 v128, v119, -v128
	v_fmaak_f32 v127, v114, v127, 0x40135761
	v_exp_f32_e32 v129, v128
	v_mul_f32_e32 v128, 0x3dd2d3e8, v115
	v_mul_f32_e64 v127, v114, -v127
	v_fmaak_f32 v128, v115, v128, 0x40135761
	v_exp_f32_e32 v127, v127
	v_mul_f32_e64 v128, v115, -v128
	v_exp_f32_e32 v131, v128
	v_mul_f32_e32 v132, 0x3dd2d3e8, v116
	v_add_f32_e32 v127, 1.0, v127
	v_rcp_f32_e32 v128, v127
	v_add_f32_e32 v127, 1.0, v129
	v_add_f32_e32 v129, 1.0, v131
	v_mul_f32_e32 v131, 0x3dd2d3e8, v120
	v_fmaak_f32 v131, v120, v131, 0x40135761
	v_mul_f32_e64 v131, v120, -v131
	v_fmaak_f32 v132, v116, v132, 0x40135761
	v_exp_f32_e32 v131, v131
	v_mul_f32_e64 v132, v116, -v132
	v_exp_f32_e32 v133, v132
	v_mul_f32_e32 v126, 0x3dd2d3e8, v118
	v_add_f32_e32 v131, 1.0, v131
	v_rcp_f32_e32 v132, v131
	v_add_f32_e32 v131, 1.0, v133
	v_mul_f32_e32 v133, 0x3dd2d3e8, v121
	v_fmaak_f32 v133, v121, v133, 0x40135761
	v_mul_f32_e32 v134, 0x3dd2d3e8, v117
	v_fmaak_f32 v126, v118, v126, 0x40135761
	v_mul_f32_e64 v133, v121, -v133
	v_fmaak_f32 v134, v117, v134, 0x40135761
	v_mul_f32_e64 v126, v118, -v126
	v_exp_f32_e32 v133, v133
	v_mul_f32_e64 v134, v117, -v134
	v_exp_f32_e32 v126, v126
	v_exp_f32_e32 v135, v134
	v_rcp_f32_e32 v134, v131
	v_add_f32_e32 v131, 1.0, v133
	v_add_f32_e32 v126, 1.0, v126
	v_rcp_f32_e32 v133, v131
	v_add_f32_e32 v131, 1.0, v135
	v_rcp_f32_e32 v126, v126
	v_rcp_f32_e32 v127, v127
	v_rcp_f32_e32 v129, v129
	v_rcp_f32_e32 v135, v131
	v_pk_mul_f32 v[120:121], v[120:121], v[132:133]
	v_pk_mul_f32 v[118:119], v[118:119], v[126:127]
	v_pk_mul_f32 v[114:115], v[114:115], v[128:129]
	v_pk_mul_f32 v[116:117], v[116:117], v[134:135]
.LBB0_424:
	v_cvt_pk_bf16_f32 v118, v118, v119
	v_cvt_pk_bf16_f32 v119, v120, v121
	v_cvt_pk_bf16_f32 v121, v116, v117
	v_add_u32_e32 v116, 16, v130
	v_cvt_pk_bf16_f32 v120, v114, v115
	v_ashrrev_i32_e32 v117, 31, v116
	global_store_dwordx4 v[124:125], v[118:121], off offset:256
	v_lshl_add_u64 v[114:115], v[116:117], 2, s[22:23]
	v_mov_b32_e32 v117, v185
	v_cvt_f32_i32_e32 v111, v111
	v_cvt_f32_i32_e32 v110, v110
	v_cvt_f32_i32_e32 v107, v107
	v_cvt_f32_i32_e32 v106, v106
	v_cvt_f32_i32_e32 v119, v113
	v_cvt_f32_i32_e32 v118, v112
	v_cvt_f32_i32_e32 v121, v109
	v_cvt_f32_i32_e32 v120, v108
	s_and_b64 vcc, exec, s[4:5]
	v_mul_f32_e32 v124, v141, v117
	v_pk_mul_f32 v[112:113], v[124:125], v[110:111] op_sel_hi:[0,1]
	v_pk_mul_f32 v[108:109], v[124:125], v[106:107] op_sel_hi:[0,1]
	v_pk_mul_f32 v[118:119], v[124:125], v[118:119] op_sel_hi:[0,1]
	v_pk_mul_f32 v[110:111], v[124:125], v[120:121] op_sel_hi:[0,1]
	s_cbranch_vccnz .LBB0_426
	v_mul_f32_e32 v107, 0x3dd2d3e8, v108
	v_fmaak_f32 v107, v108, v107, 0x40135761
	v_mul_f32_e32 v117, 0x3dd2d3e8, v113
	v_mul_f32_e32 v120, 0x3dd2d3e8, v109
	v_mul_f32_e64 v107, v108, -v107
	v_fmaak_f32 v117, v113, v117, 0x40135761
	v_fmaak_f32 v120, v109, v120, 0x40135761
	v_exp_f32_e32 v107, v107
	v_mul_f32_e64 v117, v113, -v117
	v_mul_f32_e64 v120, v109, -v120
	v_exp_f32_e32 v117, v117
	v_exp_f32_e32 v121, v120
	v_add_f32_e32 v107, 1.0, v107
	v_rcp_f32_e32 v120, v107
	v_add_f32_e32 v107, 1.0, v117
	v_add_f32_e32 v117, 1.0, v121
	v_mul_f32_e32 v121, 0x3dd2d3e8, v118
	v_fmaak_f32 v121, v118, v121, 0x40135761
	v_mul_f32_e64 v121, v118, -v121
	v_exp_f32_e32 v124, v121
	v_mul_f32_e32 v121, 0x3dd2d3e8, v110
	v_fmaak_f32 v121, v110, v121, 0x40135761
	v_mul_f32_e64 v121, v110, -v121
	v_exp_f32_e32 v125, v121
	v_rcp_f32_e32 v121, v117
	v_add_f32_e32 v117, 1.0, v124
	v_rcp_f32_e32 v124, v117
	v_add_f32_e32 v117, 1.0, v125
	v_mul_f32_e32 v125, 0x3dd2d3e8, v119
	v_mul_f32_e32 v106, 0x3dd2d3e8, v112
	v_fmaak_f32 v125, v119, v125, 0x40135761
	v_mul_f32_e32 v126, 0x3dd2d3e8, v111
	v_fmaak_f32 v106, v112, v106, 0x40135761
	v_mul_f32_e64 v125, v119, -v125
	v_fmaak_f32 v126, v111, v126, 0x40135761
	v_mul_f32_e64 v106, v112, -v106
	v_exp_f32_e32 v125, v125
	v_mul_f32_e64 v126, v111, -v126
	v_exp_f32_e32 v106, v106
	v_exp_f32_e32 v127, v126
	v_rcp_f32_e32 v126, v117
	v_add_f32_e32 v117, 1.0, v125
	v_add_f32_e32 v106, 1.0, v106
	v_rcp_f32_e32 v125, v117
	v_add_f32_e32 v117, 1.0, v127
	v_rcp_f32_e32 v106, v106
	v_rcp_f32_e32 v107, v107
	v_rcp_f32_e32 v127, v117
	v_pk_mul_f32 v[118:119], v[118:119], v[124:125]
	v_pk_mul_f32 v[108:109], v[108:109], v[120:121]
	v_pk_mul_f32 v[112:113], v[112:113], v[106:107]
	v_pk_mul_f32 v[110:111], v[110:111], v[126:127]
.LBB0_426:
	v_mov_b64_e32 v[106:107], s[6:7]
	v_mad_i64_i32 v[106:107], s[28:29], v116, s57, v[106:107]
	v_lshl_add_u64 v[106:107], s[10:11], 1, v[106:107]
	v_lshl_add_u64 v[106:107], v[106:107], 0, s[20:21]
	v_lshl_add_u64 v[106:107], v[122:123], 1, v[106:107]
	v_cvt_pk_bf16_f32 v116, v112, v113
	v_cvt_pk_bf16_f32 v117, v118, v119
	v_cvt_pk_bf16_f32 v118, v108, v109
	v_cvt_pk_bf16_f32 v119, v110, v111
	global_store_dwordx4 v[106:107], v[116:119], off
	v_mov_b32_e32 v108, v185
	v_cvt_f32_i32_e32 v103, v103
	v_cvt_f32_i32_e32 v102, v102
	v_cvt_f32_i32_e32 v99, v99
	v_cvt_f32_i32_e32 v98, v98
	v_cvt_f32_i32_e32 v105, v105
	v_cvt_f32_i32_e32 v104, v104
	v_cvt_f32_i32_e32 v101, v101
	v_cvt_f32_i32_e32 v100, v100
	s_and_b64 vcc, exec, s[4:5]
	v_mul_f32_e32 v108, v141, v108
	v_pk_mul_f32 v[102:103], v[108:109], v[102:103] op_sel_hi:[0,1]
	v_pk_mul_f32 v[98:99], v[108:109], v[98:99] op_sel_hi:[0,1]
	v_pk_mul_f32 v[104:105], v[108:109], v[104:105] op_sel_hi:[0,1]
	v_pk_mul_f32 v[100:101], v[108:109], v[100:101] op_sel_hi:[0,1]
	s_cbranch_vccnz .LBB0_428
	v_mul_f32_e32 v110, 0x3dd2d3e8, v103
	v_fmaak_f32 v110, v103, v110, 0x40135761
	v_mul_f32_e32 v109, 0x3dd2d3e8, v98
	v_mul_f32_e64 v110, v103, -v110
	v_fmaak_f32 v109, v98, v109, 0x40135761
	v_exp_f32_e32 v111, v110
	v_mul_f32_e32 v110, 0x3dd2d3e8, v99
	v_mul_f32_e64 v109, v98, -v109
	v_fmaak_f32 v110, v99, v110, 0x40135761
	v_exp_f32_e32 v109, v109
	v_mul_f32_e64 v110, v99, -v110
	v_exp_f32_e32 v112, v110
	v_mul_f32_e32 v114, 0x3dd2d3e8, v105
	v_fmaak_f32 v114, v105, v114, 0x40135761
	v_add_f32_e32 v109, 1.0, v109
	v_mul_f32_e32 v113, 0x3dd2d3e8, v100
	v_mul_f32_e64 v114, v105, -v114
	v_mul_f32_e32 v108, 0x3dd2d3e8, v102
	v_rcp_f32_e32 v110, v109
	v_add_f32_e32 v109, 1.0, v111
	v_add_f32_e32 v111, 1.0, v112
	v_mul_f32_e32 v112, 0x3dd2d3e8, v104
	v_fmaak_f32 v113, v100, v113, 0x40135761
	v_exp_f32_e32 v115, v114
	v_mul_f32_e32 v114, 0x3dd2d3e8, v101
	v_fmaak_f32 v108, v102, v108, 0x40135761
	v_fmaak_f32 v112, v104, v112, 0x40135761
	v_mul_f32_e64 v113, v100, -v113
	v_fmaak_f32 v114, v101, v114, 0x40135761
	v_mul_f32_e64 v108, v102, -v108
	v_mul_f32_e64 v112, v104, -v112
	v_exp_f32_e32 v113, v113
	v_mul_f32_e64 v114, v101, -v114
	v_exp_f32_e32 v108, v108
	v_exp_f32_e32 v112, v112
	v_exp_f32_e32 v116, v114
	v_add_f32_e32 v113, 1.0, v113
	v_add_f32_e32 v108, 1.0, v108
	v_add_f32_e32 v112, 1.0, v112
	v_rcp_f32_e32 v114, v113
	v_add_f32_e32 v113, 1.0, v115
	v_add_f32_e32 v115, 1.0, v116
	v_rcp_f32_e32 v108, v108
	v_rcp_f32_e32 v109, v109
	v_rcp_f32_e32 v111, v111
	v_rcp_f32_e32 v112, v112
	v_rcp_f32_e32 v113, v113
	v_rcp_f32_e32 v115, v115
	v_pk_mul_f32 v[102:103], v[102:103], v[108:109]
	v_pk_mul_f32 v[98:99], v[98:99], v[110:111]
	v_pk_mul_f32 v[104:105], v[104:105], v[112:113]
	v_pk_mul_f32 v[100:101], v[100:101], v[114:115]
.LBB0_428:
	v_cvt_pk_bf16_f32 v102, v102, v103
	v_cvt_pk_bf16_f32 v103, v104, v105
	v_cvt_pk_bf16_f32 v105, v100, v101
	v_add_u32_e32 v100, 32, v130
	v_cvt_pk_bf16_f32 v104, v98, v99
	v_ashrrev_i32_e32 v101, 31, v100
	global_store_dwordx4 v[106:107], v[102:105], off offset:256
	v_lshl_add_u64 v[98:99], v[100:101], 2, s[22:23]
	v_mov_b32_e32 v101, v186
	v_cvt_f32_i32_e32 v95, v95
	v_cvt_f32_i32_e32 v94, v94
	v_cvt_f32_i32_e32 v91, v91
	v_cvt_f32_i32_e32 v90, v90
	v_cvt_f32_i32_e32 v103, v97
	v_cvt_f32_i32_e32 v102, v96
	v_cvt_f32_i32_e32 v105, v93
	v_cvt_f32_i32_e32 v104, v92
	s_and_b64 vcc, exec, s[4:5]
	v_mul_f32_e32 v106, v141, v101
	v_pk_mul_f32 v[96:97], v[106:107], v[94:95] op_sel_hi:[0,1]
	v_pk_mul_f32 v[92:93], v[106:107], v[90:91] op_sel_hi:[0,1]
	v_pk_mul_f32 v[102:103], v[106:107], v[102:103] op_sel_hi:[0,1]
	v_pk_mul_f32 v[94:95], v[106:107], v[104:105] op_sel_hi:[0,1]
	s_cbranch_vccnz .LBB0_430
	v_mul_f32_e32 v91, 0x3dd2d3e8, v92
	v_fmaak_f32 v91, v92, v91, 0x40135761
	v_mul_f32_e32 v101, 0x3dd2d3e8, v97
	v_mul_f32_e32 v104, 0x3dd2d3e8, v93
	v_mul_f32_e64 v91, v92, -v91
	v_fmaak_f32 v101, v97, v101, 0x40135761
	v_fmaak_f32 v104, v93, v104, 0x40135761
	v_exp_f32_e32 v91, v91
	v_mul_f32_e64 v101, v97, -v101
	v_mul_f32_e64 v104, v93, -v104
	v_exp_f32_e32 v101, v101
	v_exp_f32_e32 v105, v104
	v_add_f32_e32 v91, 1.0, v91
	v_rcp_f32_e32 v104, v91
	v_add_f32_e32 v91, 1.0, v101
	v_add_f32_e32 v101, 1.0, v105
	v_mul_f32_e32 v105, 0x3dd2d3e8, v102
	v_fmaak_f32 v105, v102, v105, 0x40135761
	v_mul_f32_e64 v105, v102, -v105
	v_exp_f32_e32 v106, v105
	v_mul_f32_e32 v105, 0x3dd2d3e8, v94
	v_fmaak_f32 v105, v94, v105, 0x40135761
	v_mul_f32_e64 v105, v94, -v105
	v_exp_f32_e32 v107, v105
	v_rcp_f32_e32 v105, v101
	v_add_f32_e32 v101, 1.0, v106
	v_rcp_f32_e32 v106, v101
	v_add_f32_e32 v101, 1.0, v107
	v_mul_f32_e32 v107, 0x3dd2d3e8, v103
	v_mul_f32_e32 v90, 0x3dd2d3e8, v96
	v_fmaak_f32 v107, v103, v107, 0x40135761
	v_mul_f32_e32 v108, 0x3dd2d3e8, v95
	v_fmaak_f32 v90, v96, v90, 0x40135761
	v_mul_f32_e64 v107, v103, -v107
	v_fmaak_f32 v108, v95, v108, 0x40135761
	v_mul_f32_e64 v90, v96, -v90
	v_exp_f32_e32 v107, v107
	v_mul_f32_e64 v108, v95, -v108
	v_exp_f32_e32 v90, v90
	v_exp_f32_e32 v109, v108
	v_rcp_f32_e32 v108, v101
	v_add_f32_e32 v101, 1.0, v107
	v_add_f32_e32 v90, 1.0, v90
	v_rcp_f32_e32 v107, v101
	v_add_f32_e32 v101, 1.0, v109
	v_rcp_f32_e32 v90, v90
	v_rcp_f32_e32 v91, v91
	v_rcp_f32_e32 v109, v101
	v_pk_mul_f32 v[102:103], v[102:103], v[106:107]
	v_pk_mul_f32 v[92:93], v[92:93], v[104:105]
	v_pk_mul_f32 v[96:97], v[96:97], v[90:91]
	v_pk_mul_f32 v[94:95], v[94:95], v[108:109]
.LBB0_430:
	v_mov_b64_e32 v[90:91], s[6:7]
	v_mad_i64_i32 v[90:91], s[28:29], v100, s57, v[90:91]
	v_lshl_add_u64 v[90:91], s[10:11], 1, v[90:91]
	v_lshl_add_u64 v[90:91], v[90:91], 0, s[20:21]
	v_lshl_add_u64 v[90:91], v[122:123], 1, v[90:91]
	v_cvt_pk_bf16_f32 v100, v96, v97
	v_cvt_pk_bf16_f32 v101, v102, v103
	v_cvt_pk_bf16_f32 v102, v92, v93
	v_cvt_pk_bf16_f32 v103, v94, v95
	global_store_dwordx4 v[90:91], v[100:103], off
	v_mov_b32_e32 v92, v186
	v_cvt_f32_i32_e32 v87, v87
	v_cvt_f32_i32_e32 v86, v86
	v_cvt_f32_i32_e32 v83, v83
	v_cvt_f32_i32_e32 v82, v82
	v_cvt_f32_i32_e32 v89, v89
	v_cvt_f32_i32_e32 v88, v88
	v_cvt_f32_i32_e32 v85, v85
	v_cvt_f32_i32_e32 v84, v84
	s_and_b64 vcc, exec, s[4:5]
	v_mul_f32_e32 v92, v141, v92
	v_pk_mul_f32 v[86:87], v[92:93], v[86:87] op_sel_hi:[0,1]
	v_pk_mul_f32 v[82:83], v[92:93], v[82:83] op_sel_hi:[0,1]
	v_pk_mul_f32 v[88:89], v[92:93], v[88:89] op_sel_hi:[0,1]
	v_pk_mul_f32 v[84:85], v[92:93], v[84:85] op_sel_hi:[0,1]
	s_cbranch_vccnz .LBB0_432
	v_mul_f32_e32 v94, 0x3dd2d3e8, v87
	v_fmaak_f32 v94, v87, v94, 0x40135761
	v_mul_f32_e32 v93, 0x3dd2d3e8, v82
	v_mul_f32_e64 v94, v87, -v94
	v_fmaak_f32 v93, v82, v93, 0x40135761
	v_exp_f32_e32 v95, v94
	v_mul_f32_e32 v94, 0x3dd2d3e8, v83
	v_mul_f32_e64 v93, v82, -v93
	v_fmaak_f32 v94, v83, v94, 0x40135761
	v_exp_f32_e32 v93, v93
	v_mul_f32_e64 v94, v83, -v94
	v_exp_f32_e32 v96, v94
	v_mul_f32_e32 v98, 0x3dd2d3e8, v89
	v_fmaak_f32 v98, v89, v98, 0x40135761
	v_add_f32_e32 v93, 1.0, v93
	v_mul_f32_e32 v97, 0x3dd2d3e8, v84
	v_mul_f32_e64 v98, v89, -v98
	v_mul_f32_e32 v92, 0x3dd2d3e8, v86
	v_rcp_f32_e32 v94, v93
	v_add_f32_e32 v93, 1.0, v95
	v_add_f32_e32 v95, 1.0, v96
	v_mul_f32_e32 v96, 0x3dd2d3e8, v88
	v_fmaak_f32 v97, v84, v97, 0x40135761
	v_exp_f32_e32 v99, v98
	v_mul_f32_e32 v98, 0x3dd2d3e8, v85
	v_fmaak_f32 v92, v86, v92, 0x40135761
	v_fmaak_f32 v96, v88, v96, 0x40135761
	v_mul_f32_e64 v97, v84, -v97
	v_fmaak_f32 v98, v85, v98, 0x40135761
	v_mul_f32_e64 v92, v86, -v92
	v_mul_f32_e64 v96, v88, -v96
	v_exp_f32_e32 v97, v97
	v_mul_f32_e64 v98, v85, -v98
	v_exp_f32_e32 v92, v92
	v_exp_f32_e32 v96, v96
	v_exp_f32_e32 v100, v98
	v_add_f32_e32 v97, 1.0, v97
	v_add_f32_e32 v92, 1.0, v92
	v_add_f32_e32 v96, 1.0, v96
	v_rcp_f32_e32 v98, v97
	v_add_f32_e32 v97, 1.0, v99
	v_add_f32_e32 v99, 1.0, v100
	v_rcp_f32_e32 v92, v92
	v_rcp_f32_e32 v93, v93
	v_rcp_f32_e32 v95, v95
	v_rcp_f32_e32 v96, v96
	v_rcp_f32_e32 v97, v97
	v_rcp_f32_e32 v99, v99
	v_pk_mul_f32 v[86:87], v[86:87], v[92:93]
	v_pk_mul_f32 v[82:83], v[82:83], v[94:95]
	v_pk_mul_f32 v[88:89], v[88:89], v[96:97]
	v_pk_mul_f32 v[84:85], v[84:85], v[98:99]
.LBB0_432:
	v_cvt_pk_bf16_f32 v86, v86, v87
	v_cvt_pk_bf16_f32 v87, v88, v89
	v_cvt_pk_bf16_f32 v89, v84, v85
	v_add_u32_e32 v84, 48, v130
	v_cvt_pk_bf16_f32 v88, v82, v83
	v_ashrrev_i32_e32 v85, 31, v84
	global_store_dwordx4 v[90:91], v[86:89], off offset:256
	v_lshl_add_u64 v[82:83], v[84:85], 2, s[22:23]
	v_mov_b32_e32 v85, v187
	v_cvt_f32_i32_e32 v79, v79
	v_cvt_f32_i32_e32 v78, v78
	v_cvt_f32_i32_e32 v75, v75
	v_cvt_f32_i32_e32 v74, v74
	v_cvt_f32_i32_e32 v87, v81
	v_cvt_f32_i32_e32 v86, v80
	v_cvt_f32_i32_e32 v89, v77
	v_cvt_f32_i32_e32 v88, v76
	s_and_b64 vcc, exec, s[4:5]
	v_mul_f32_e32 v90, v141, v85
	v_pk_mul_f32 v[80:81], v[90:91], v[78:79] op_sel_hi:[0,1]
	v_pk_mul_f32 v[76:77], v[90:91], v[74:75] op_sel_hi:[0,1]
	v_pk_mul_f32 v[86:87], v[90:91], v[86:87] op_sel_hi:[0,1]
	v_pk_mul_f32 v[78:79], v[90:91], v[88:89] op_sel_hi:[0,1]
	s_cbranch_vccnz .LBB0_434
	v_mul_f32_e32 v75, 0x3dd2d3e8, v76
	v_fmaak_f32 v75, v76, v75, 0x40135761
	v_mul_f32_e32 v85, 0x3dd2d3e8, v81
	v_mul_f32_e32 v88, 0x3dd2d3e8, v77
	v_mul_f32_e64 v75, v76, -v75
	v_fmaak_f32 v85, v81, v85, 0x40135761
	v_fmaak_f32 v88, v77, v88, 0x40135761
	v_exp_f32_e32 v75, v75
	v_mul_f32_e64 v85, v81, -v85
	v_mul_f32_e64 v88, v77, -v88
	v_exp_f32_e32 v85, v85
	v_exp_f32_e32 v89, v88
	v_add_f32_e32 v75, 1.0, v75
	v_rcp_f32_e32 v88, v75
	v_add_f32_e32 v75, 1.0, v85
	v_add_f32_e32 v85, 1.0, v89
	v_mul_f32_e32 v89, 0x3dd2d3e8, v86
	v_fmaak_f32 v89, v86, v89, 0x40135761
	v_mul_f32_e64 v89, v86, -v89
	v_exp_f32_e32 v90, v89
	v_mul_f32_e32 v89, 0x3dd2d3e8, v78
	v_fmaak_f32 v89, v78, v89, 0x40135761
	v_mul_f32_e64 v89, v78, -v89
	v_exp_f32_e32 v91, v89
	v_rcp_f32_e32 v89, v85
	v_add_f32_e32 v85, 1.0, v90
	v_rcp_f32_e32 v90, v85
	v_add_f32_e32 v85, 1.0, v91
	v_mul_f32_e32 v91, 0x3dd2d3e8, v87
	v_mul_f32_e32 v74, 0x3dd2d3e8, v80
	v_fmaak_f32 v91, v87, v91, 0x40135761
	v_mul_f32_e32 v92, 0x3dd2d3e8, v79
	v_fmaak_f32 v74, v80, v74, 0x40135761
	v_mul_f32_e64 v91, v87, -v91
	v_fmaak_f32 v92, v79, v92, 0x40135761
	v_mul_f32_e64 v74, v80, -v74
	v_exp_f32_e32 v91, v91
	v_mul_f32_e64 v92, v79, -v92
	v_exp_f32_e32 v74, v74
	v_exp_f32_e32 v93, v92
	v_rcp_f32_e32 v92, v85
	v_add_f32_e32 v85, 1.0, v91
	v_add_f32_e32 v74, 1.0, v74
	v_rcp_f32_e32 v91, v85
	v_add_f32_e32 v85, 1.0, v93
	v_rcp_f32_e32 v74, v74
	v_rcp_f32_e32 v75, v75
	v_rcp_f32_e32 v93, v85
	v_pk_mul_f32 v[86:87], v[86:87], v[90:91]
	v_pk_mul_f32 v[76:77], v[76:77], v[88:89]
	v_pk_mul_f32 v[80:81], v[80:81], v[74:75]
	v_pk_mul_f32 v[78:79], v[78:79], v[92:93]
.LBB0_434:
	v_mov_b64_e32 v[74:75], s[6:7]
	v_mad_i64_i32 v[74:75], s[28:29], v84, s57, v[74:75]
	v_lshl_add_u64 v[74:75], s[10:11], 1, v[74:75]
	v_lshl_add_u64 v[74:75], v[74:75], 0, s[20:21]
	v_lshl_add_u64 v[74:75], v[122:123], 1, v[74:75]
	v_cvt_pk_bf16_f32 v84, v80, v81
	v_cvt_pk_bf16_f32 v85, v86, v87
	v_cvt_pk_bf16_f32 v86, v76, v77
	v_cvt_pk_bf16_f32 v87, v78, v79
	global_store_dwordx4 v[74:75], v[84:87], off
	v_mov_b32_e32 v76, v187
	v_cvt_f32_i32_e32 v71, v71
	v_cvt_f32_i32_e32 v70, v70
	v_cvt_f32_i32_e32 v67, v67
	v_cvt_f32_i32_e32 v66, v66
	v_cvt_f32_i32_e32 v73, v73
	v_cvt_f32_i32_e32 v72, v72
	v_cvt_f32_i32_e32 v69, v69
	v_cvt_f32_i32_e32 v68, v68
	s_and_b64 vcc, exec, s[4:5]
	v_mul_f32_e32 v76, v141, v76
	v_pk_mul_f32 v[70:71], v[76:77], v[70:71] op_sel_hi:[0,1]
	v_pk_mul_f32 v[66:67], v[76:77], v[66:67] op_sel_hi:[0,1]
	v_pk_mul_f32 v[72:73], v[76:77], v[72:73] op_sel_hi:[0,1]
	v_pk_mul_f32 v[68:69], v[76:77], v[68:69] op_sel_hi:[0,1]
	s_cbranch_vccnz .LBB0_436
	v_mul_f32_e32 v78, 0x3dd2d3e8, v71
	v_fmaak_f32 v78, v71, v78, 0x40135761
	v_mul_f32_e32 v77, 0x3dd2d3e8, v66
	v_mul_f32_e64 v78, v71, -v78
	v_fmaak_f32 v77, v66, v77, 0x40135761
	v_exp_f32_e32 v79, v78
	v_mul_f32_e32 v78, 0x3dd2d3e8, v67
	v_mul_f32_e64 v77, v66, -v77
	v_fmaak_f32 v78, v67, v78, 0x40135761
	v_exp_f32_e32 v77, v77
	v_mul_f32_e64 v78, v67, -v78
	v_exp_f32_e32 v80, v78
	v_mul_f32_e32 v82, 0x3dd2d3e8, v73
	v_fmaak_f32 v82, v73, v82, 0x40135761
	v_add_f32_e32 v77, 1.0, v77
	v_mul_f32_e32 v81, 0x3dd2d3e8, v68
	v_mul_f32_e64 v82, v73, -v82
	v_mul_f32_e32 v76, 0x3dd2d3e8, v70
	v_rcp_f32_e32 v78, v77
	v_add_f32_e32 v77, 1.0, v79
	v_add_f32_e32 v79, 1.0, v80
	v_mul_f32_e32 v80, 0x3dd2d3e8, v72
	v_fmaak_f32 v81, v68, v81, 0x40135761
	v_exp_f32_e32 v83, v82
	v_mul_f32_e32 v82, 0x3dd2d3e8, v69
	v_fmaak_f32 v76, v70, v76, 0x40135761
	v_fmaak_f32 v80, v72, v80, 0x40135761
	v_mul_f32_e64 v81, v68, -v81
	v_fmaak_f32 v82, v69, v82, 0x40135761
	v_mul_f32_e64 v76, v70, -v76
	v_mul_f32_e64 v80, v72, -v80
	v_exp_f32_e32 v81, v81
	v_mul_f32_e64 v82, v69, -v82
	v_exp_f32_e32 v76, v76
	v_exp_f32_e32 v80, v80
	v_exp_f32_e32 v84, v82
	v_add_f32_e32 v81, 1.0, v81
	v_add_f32_e32 v76, 1.0, v76
	v_add_f32_e32 v80, 1.0, v80
	v_rcp_f32_e32 v82, v81
	v_add_f32_e32 v81, 1.0, v83
	v_add_f32_e32 v83, 1.0, v84
	v_rcp_f32_e32 v76, v76
	v_rcp_f32_e32 v77, v77
	v_rcp_f32_e32 v79, v79
	v_rcp_f32_e32 v80, v80
	v_rcp_f32_e32 v81, v81
	v_rcp_f32_e32 v83, v83
	v_pk_mul_f32 v[70:71], v[70:71], v[76:77]
	v_pk_mul_f32 v[66:67], v[66:67], v[78:79]
	v_pk_mul_f32 v[72:73], v[72:73], v[80:81]
	v_pk_mul_f32 v[68:69], v[68:69], v[82:83]
.LBB0_436:
	v_cvt_pk_bf16_f32 v70, v70, v71
	v_cvt_pk_bf16_f32 v71, v72, v73
	v_cvt_pk_bf16_f32 v73, v68, v69
	v_add_u32_e32 v68, 0x80, v130
	v_cvt_pk_bf16_f32 v72, v66, v67
	v_ashrrev_i32_e32 v69, 31, v68
	global_store_dwordx4 v[74:75], v[70:73], off offset:256
	v_lshl_add_u64 v[66:67], v[68:69], 2, s[22:23]
	v_mov_b32_e32 v69, v188
	v_cvt_f32_i32_e32 v63, v63
	v_cvt_f32_i32_e32 v62, v62
	v_cvt_f32_i32_e32 v59, v59
	v_cvt_f32_i32_e32 v58, v58
	v_cvt_f32_i32_e32 v71, v65
	v_cvt_f32_i32_e32 v70, v64
	v_cvt_f32_i32_e32 v73, v61
	v_cvt_f32_i32_e32 v72, v60
	s_and_b64 vcc, exec, s[4:5]
	v_mul_f32_e32 v74, v141, v69
	v_pk_mul_f32 v[64:65], v[74:75], v[62:63] op_sel_hi:[0,1]
	v_pk_mul_f32 v[60:61], v[74:75], v[58:59] op_sel_hi:[0,1]
	v_pk_mul_f32 v[70:71], v[74:75], v[70:71] op_sel_hi:[0,1]
	v_pk_mul_f32 v[62:63], v[74:75], v[72:73] op_sel_hi:[0,1]
	s_cbranch_vccnz .LBB0_438
	v_mul_f32_e32 v59, 0x3dd2d3e8, v60
	v_fmaak_f32 v59, v60, v59, 0x40135761
	v_mul_f32_e32 v69, 0x3dd2d3e8, v65
	v_mul_f32_e32 v72, 0x3dd2d3e8, v61
	v_mul_f32_e64 v59, v60, -v59
	v_fmaak_f32 v69, v65, v69, 0x40135761
	v_fmaak_f32 v72, v61, v72, 0x40135761
	v_exp_f32_e32 v59, v59
	v_mul_f32_e64 v69, v65, -v69
	v_mul_f32_e64 v72, v61, -v72
	v_exp_f32_e32 v69, v69
	v_exp_f32_e32 v73, v72
	v_add_f32_e32 v59, 1.0, v59
	v_rcp_f32_e32 v72, v59
	v_add_f32_e32 v59, 1.0, v69
	v_add_f32_e32 v69, 1.0, v73
	v_mul_f32_e32 v73, 0x3dd2d3e8, v70
	v_fmaak_f32 v73, v70, v73, 0x40135761
	v_mul_f32_e64 v73, v70, -v73
	v_exp_f32_e32 v74, v73
	v_mul_f32_e32 v73, 0x3dd2d3e8, v62
	v_fmaak_f32 v73, v62, v73, 0x40135761
	v_mul_f32_e64 v73, v62, -v73
	v_exp_f32_e32 v75, v73
	v_rcp_f32_e32 v73, v69
	v_add_f32_e32 v69, 1.0, v74
	v_rcp_f32_e32 v74, v69
	v_add_f32_e32 v69, 1.0, v75
	v_mul_f32_e32 v75, 0x3dd2d3e8, v71
	v_mul_f32_e32 v58, 0x3dd2d3e8, v64
	v_fmaak_f32 v75, v71, v75, 0x40135761
	v_mul_f32_e32 v76, 0x3dd2d3e8, v63
	v_fmaak_f32 v58, v64, v58, 0x40135761
	v_mul_f32_e64 v75, v71, -v75
	v_fmaak_f32 v76, v63, v76, 0x40135761
	v_mul_f32_e64 v58, v64, -v58
	v_exp_f32_e32 v75, v75
	v_mul_f32_e64 v76, v63, -v76
	v_exp_f32_e32 v58, v58
	v_exp_f32_e32 v77, v76
	v_rcp_f32_e32 v76, v69
	v_add_f32_e32 v69, 1.0, v75
	v_add_f32_e32 v58, 1.0, v58
	v_rcp_f32_e32 v75, v69
	v_add_f32_e32 v69, 1.0, v77
	v_rcp_f32_e32 v58, v58
	v_rcp_f32_e32 v59, v59
	v_rcp_f32_e32 v77, v69
	v_pk_mul_f32 v[70:71], v[70:71], v[74:75]
	v_pk_mul_f32 v[60:61], v[60:61], v[72:73]
	v_pk_mul_f32 v[64:65], v[64:65], v[58:59]
	v_pk_mul_f32 v[62:63], v[62:63], v[76:77]
.LBB0_438:
	v_mov_b64_e32 v[58:59], s[6:7]
	v_mad_i64_i32 v[58:59], s[28:29], v68, s57, v[58:59]
	v_lshl_add_u64 v[58:59], s[10:11], 1, v[58:59]
	v_lshl_add_u64 v[58:59], v[58:59], 0, s[20:21]
	v_lshl_add_u64 v[58:59], v[122:123], 1, v[58:59]
	v_cvt_pk_bf16_f32 v68, v64, v65
	v_cvt_pk_bf16_f32 v69, v70, v71
	v_cvt_pk_bf16_f32 v70, v60, v61
	v_cvt_pk_bf16_f32 v71, v62, v63
	global_store_dwordx4 v[58:59], v[68:71], off
	v_mov_b32_e32 v60, v188
	v_cvt_f32_i32_e32 v55, v55
	v_cvt_f32_i32_e32 v54, v54
	v_cvt_f32_i32_e32 v51, v51
	v_cvt_f32_i32_e32 v50, v50
	v_cvt_f32_i32_e32 v57, v57
	v_cvt_f32_i32_e32 v56, v56
	v_cvt_f32_i32_e32 v53, v53
	v_cvt_f32_i32_e32 v52, v52
	s_and_b64 vcc, exec, s[4:5]
	v_mul_f32_e32 v60, v141, v60
	v_pk_mul_f32 v[54:55], v[60:61], v[54:55] op_sel_hi:[0,1]
	v_pk_mul_f32 v[50:51], v[60:61], v[50:51] op_sel_hi:[0,1]
	v_pk_mul_f32 v[56:57], v[60:61], v[56:57] op_sel_hi:[0,1]
	v_pk_mul_f32 v[52:53], v[60:61], v[52:53] op_sel_hi:[0,1]
	s_cbranch_vccnz .LBB0_440
	v_mul_f32_e32 v62, 0x3dd2d3e8, v55
	v_fmaak_f32 v62, v55, v62, 0x40135761
	v_mul_f32_e32 v61, 0x3dd2d3e8, v50
	v_mul_f32_e64 v62, v55, -v62
	v_fmaak_f32 v61, v50, v61, 0x40135761
	v_exp_f32_e32 v63, v62
	v_mul_f32_e32 v62, 0x3dd2d3e8, v51
	v_mul_f32_e64 v61, v50, -v61
	v_fmaak_f32 v62, v51, v62, 0x40135761
	v_exp_f32_e32 v61, v61
	v_mul_f32_e64 v62, v51, -v62
	v_exp_f32_e32 v64, v62
	v_mul_f32_e32 v66, 0x3dd2d3e8, v57
	v_fmaak_f32 v66, v57, v66, 0x40135761
	v_add_f32_e32 v61, 1.0, v61
	v_mul_f32_e32 v65, 0x3dd2d3e8, v52
	v_mul_f32_e64 v66, v57, -v66
	v_mul_f32_e32 v60, 0x3dd2d3e8, v54
	v_rcp_f32_e32 v62, v61
	v_add_f32_e32 v61, 1.0, v63
	v_add_f32_e32 v63, 1.0, v64
	v_mul_f32_e32 v64, 0x3dd2d3e8, v56
	v_fmaak_f32 v65, v52, v65, 0x40135761
	v_exp_f32_e32 v67, v66
	v_mul_f32_e32 v66, 0x3dd2d3e8, v53
	v_fmaak_f32 v60, v54, v60, 0x40135761
	v_fmaak_f32 v64, v56, v64, 0x40135761
	v_mul_f32_e64 v65, v52, -v65
	v_fmaak_f32 v66, v53, v66, 0x40135761
	v_mul_f32_e64 v60, v54, -v60
	v_mul_f32_e64 v64, v56, -v64
	v_exp_f32_e32 v65, v65
	v_mul_f32_e64 v66, v53, -v66
	v_exp_f32_e32 v60, v60
	v_exp_f32_e32 v64, v64
	v_exp_f32_e32 v68, v66
	v_add_f32_e32 v65, 1.0, v65
	v_add_f32_e32 v60, 1.0, v60
	v_add_f32_e32 v64, 1.0, v64
	v_rcp_f32_e32 v66, v65
	v_add_f32_e32 v65, 1.0, v67
	v_add_f32_e32 v67, 1.0, v68
	v_rcp_f32_e32 v60, v60
	v_rcp_f32_e32 v61, v61
	v_rcp_f32_e32 v63, v63
	v_rcp_f32_e32 v64, v64
	v_rcp_f32_e32 v65, v65
	v_rcp_f32_e32 v67, v67
	v_pk_mul_f32 v[54:55], v[54:55], v[60:61]
	v_pk_mul_f32 v[50:51], v[50:51], v[62:63]
	v_pk_mul_f32 v[56:57], v[56:57], v[64:65]
	v_pk_mul_f32 v[52:53], v[52:53], v[66:67]
.LBB0_440:
	v_cvt_pk_bf16_f32 v54, v54, v55
	v_cvt_pk_bf16_f32 v55, v56, v57
	v_cvt_pk_bf16_f32 v57, v52, v53
	v_add_u32_e32 v52, 0x90, v130
	v_cvt_pk_bf16_f32 v56, v50, v51
	v_ashrrev_i32_e32 v53, 31, v52
	global_store_dwordx4 v[58:59], v[54:57], off offset:256
	v_lshl_add_u64 v[50:51], v[52:53], 2, s[22:23]
	v_mov_b32_e32 v53, v189
	v_cvt_f32_i32_e32 v47, v47
	v_cvt_f32_i32_e32 v46, v46
	v_cvt_f32_i32_e32 v43, v43
	v_cvt_f32_i32_e32 v42, v42
	v_cvt_f32_i32_e32 v55, v49
	v_cvt_f32_i32_e32 v54, v48
	v_cvt_f32_i32_e32 v57, v45
	v_cvt_f32_i32_e32 v56, v44
	s_and_b64 vcc, exec, s[4:5]
	v_mul_f32_e32 v58, v141, v53
	v_pk_mul_f32 v[48:49], v[58:59], v[46:47] op_sel_hi:[0,1]
	v_pk_mul_f32 v[44:45], v[58:59], v[42:43] op_sel_hi:[0,1]
	v_pk_mul_f32 v[54:55], v[58:59], v[54:55] op_sel_hi:[0,1]
	v_pk_mul_f32 v[46:47], v[58:59], v[56:57] op_sel_hi:[0,1]
	s_cbranch_vccnz .LBB0_442
	v_mul_f32_e32 v43, 0x3dd2d3e8, v44
	v_fmaak_f32 v43, v44, v43, 0x40135761
	v_mul_f32_e32 v53, 0x3dd2d3e8, v49
	v_mul_f32_e32 v56, 0x3dd2d3e8, v45
	v_mul_f32_e64 v43, v44, -v43
	v_fmaak_f32 v53, v49, v53, 0x40135761
	v_fmaak_f32 v56, v45, v56, 0x40135761
	v_exp_f32_e32 v43, v43
	v_mul_f32_e64 v53, v49, -v53
	v_mul_f32_e64 v56, v45, -v56
	v_exp_f32_e32 v53, v53
	v_exp_f32_e32 v57, v56
	v_add_f32_e32 v43, 1.0, v43
	v_rcp_f32_e32 v56, v43
	v_add_f32_e32 v43, 1.0, v53
	v_add_f32_e32 v53, 1.0, v57
	v_mul_f32_e32 v57, 0x3dd2d3e8, v54
	v_fmaak_f32 v57, v54, v57, 0x40135761
	v_mul_f32_e64 v57, v54, -v57
	v_exp_f32_e32 v58, v57
	v_mul_f32_e32 v57, 0x3dd2d3e8, v46
	v_fmaak_f32 v57, v46, v57, 0x40135761
	v_mul_f32_e64 v57, v46, -v57
	v_exp_f32_e32 v59, v57
	v_rcp_f32_e32 v57, v53
	v_add_f32_e32 v53, 1.0, v58
	v_rcp_f32_e32 v58, v53
	v_add_f32_e32 v53, 1.0, v59
	v_mul_f32_e32 v59, 0x3dd2d3e8, v55
	v_mul_f32_e32 v42, 0x3dd2d3e8, v48
	v_fmaak_f32 v59, v55, v59, 0x40135761
	v_mul_f32_e32 v60, 0x3dd2d3e8, v47
	v_fmaak_f32 v42, v48, v42, 0x40135761
	v_mul_f32_e64 v59, v55, -v59
	v_fmaak_f32 v60, v47, v60, 0x40135761
	v_mul_f32_e64 v42, v48, -v42
	v_exp_f32_e32 v59, v59
	v_mul_f32_e64 v60, v47, -v60
	v_exp_f32_e32 v42, v42
	v_exp_f32_e32 v61, v60
	v_rcp_f32_e32 v60, v53
	v_add_f32_e32 v53, 1.0, v59
	v_add_f32_e32 v42, 1.0, v42
	v_rcp_f32_e32 v59, v53
	v_add_f32_e32 v53, 1.0, v61
	v_rcp_f32_e32 v42, v42
	v_rcp_f32_e32 v43, v43
	v_rcp_f32_e32 v61, v53
	v_pk_mul_f32 v[54:55], v[54:55], v[58:59]
	v_pk_mul_f32 v[44:45], v[44:45], v[56:57]
	v_pk_mul_f32 v[48:49], v[48:49], v[42:43]
	v_pk_mul_f32 v[46:47], v[46:47], v[60:61]
.LBB0_442:
	v_mov_b64_e32 v[42:43], s[6:7]
	v_mad_i64_i32 v[42:43], s[28:29], v52, s57, v[42:43]
	v_lshl_add_u64 v[42:43], s[10:11], 1, v[42:43]
	v_lshl_add_u64 v[42:43], v[42:43], 0, s[20:21]
	v_lshl_add_u64 v[42:43], v[122:123], 1, v[42:43]
	v_cvt_pk_bf16_f32 v52, v48, v49
	v_cvt_pk_bf16_f32 v53, v54, v55
	v_cvt_pk_bf16_f32 v54, v44, v45
	v_cvt_pk_bf16_f32 v55, v46, v47
	global_store_dwordx4 v[42:43], v[52:55], off
	v_mov_b32_e32 v44, v189
	v_cvt_f32_i32_e32 v39, v39
	v_cvt_f32_i32_e32 v38, v38
	v_cvt_f32_i32_e32 v35, v35
	v_cvt_f32_i32_e32 v34, v34
	v_cvt_f32_i32_e32 v41, v41
	v_cvt_f32_i32_e32 v40, v40
	v_cvt_f32_i32_e32 v37, v37
	v_cvt_f32_i32_e32 v36, v36
	s_and_b64 vcc, exec, s[4:5]
	v_mul_f32_e32 v44, v141, v44
	v_pk_mul_f32 v[38:39], v[44:45], v[38:39] op_sel_hi:[0,1]
	v_pk_mul_f32 v[34:35], v[44:45], v[34:35] op_sel_hi:[0,1]
	v_pk_mul_f32 v[40:41], v[44:45], v[40:41] op_sel_hi:[0,1]
	v_pk_mul_f32 v[36:37], v[44:45], v[36:37] op_sel_hi:[0,1]
	s_cbranch_vccnz .LBB0_444
	v_mul_f32_e32 v46, 0x3dd2d3e8, v39
	v_fmaak_f32 v46, v39, v46, 0x40135761
	v_mul_f32_e32 v45, 0x3dd2d3e8, v34
	v_mul_f32_e64 v46, v39, -v46
	v_fmaak_f32 v45, v34, v45, 0x40135761
	v_exp_f32_e32 v47, v46
	v_mul_f32_e32 v46, 0x3dd2d3e8, v35
	v_mul_f32_e64 v45, v34, -v45
	v_fmaak_f32 v46, v35, v46, 0x40135761
	v_exp_f32_e32 v45, v45
	v_mul_f32_e64 v46, v35, -v46
	v_exp_f32_e32 v48, v46
	v_mul_f32_e32 v50, 0x3dd2d3e8, v41
	v_fmaak_f32 v50, v41, v50, 0x40135761
	v_add_f32_e32 v45, 1.0, v45
	v_mul_f32_e32 v49, 0x3dd2d3e8, v36
	v_mul_f32_e64 v50, v41, -v50
	v_mul_f32_e32 v44, 0x3dd2d3e8, v38
	v_rcp_f32_e32 v46, v45
	v_add_f32_e32 v45, 1.0, v47
	v_add_f32_e32 v47, 1.0, v48
	v_mul_f32_e32 v48, 0x3dd2d3e8, v40
	v_fmaak_f32 v49, v36, v49, 0x40135761
	v_exp_f32_e32 v51, v50
	v_mul_f32_e32 v50, 0x3dd2d3e8, v37
	v_fmaak_f32 v44, v38, v44, 0x40135761
	v_fmaak_f32 v48, v40, v48, 0x40135761
	v_mul_f32_e64 v49, v36, -v49
	v_fmaak_f32 v50, v37, v50, 0x40135761
	v_mul_f32_e64 v44, v38, -v44
	v_mul_f32_e64 v48, v40, -v48
	v_exp_f32_e32 v49, v49
	v_mul_f32_e64 v50, v37, -v50
	v_exp_f32_e32 v44, v44
	v_exp_f32_e32 v48, v48
	v_exp_f32_e32 v52, v50
	v_add_f32_e32 v49, 1.0, v49
	v_add_f32_e32 v44, 1.0, v44
	v_add_f32_e32 v48, 1.0, v48
	v_rcp_f32_e32 v50, v49
	v_add_f32_e32 v49, 1.0, v51
	v_add_f32_e32 v51, 1.0, v52
	v_rcp_f32_e32 v44, v44
	v_rcp_f32_e32 v45, v45
	v_rcp_f32_e32 v47, v47
	v_rcp_f32_e32 v48, v48
	v_rcp_f32_e32 v49, v49
	v_rcp_f32_e32 v51, v51
	v_pk_mul_f32 v[38:39], v[38:39], v[44:45]
	v_pk_mul_f32 v[34:35], v[34:35], v[46:47]
	v_pk_mul_f32 v[40:41], v[40:41], v[48:49]
	v_pk_mul_f32 v[36:37], v[36:37], v[50:51]
.LBB0_444:
	v_cvt_pk_bf16_f32 v38, v38, v39
	v_cvt_pk_bf16_f32 v39, v40, v41
	v_cvt_pk_bf16_f32 v41, v36, v37
	v_add_u32_e32 v36, 0xa0, v130
	v_cvt_pk_bf16_f32 v40, v34, v35
	v_ashrrev_i32_e32 v37, 31, v36
	global_store_dwordx4 v[42:43], v[38:41], off offset:256
	v_lshl_add_u64 v[34:35], v[36:37], 2, s[22:23]
	v_mov_b32_e32 v37, v190
	v_cvt_f32_i32_e32 v31, v31
	v_cvt_f32_i32_e32 v30, v30
	v_cvt_f32_i32_e32 v27, v27
	v_cvt_f32_i32_e32 v26, v26
	v_cvt_f32_i32_e32 v39, v33
	v_cvt_f32_i32_e32 v38, v32
	v_cvt_f32_i32_e32 v41, v29
	v_cvt_f32_i32_e32 v40, v28
	s_and_b64 vcc, exec, s[4:5]
	v_mul_f32_e32 v42, v141, v37
	v_pk_mul_f32 v[32:33], v[42:43], v[30:31] op_sel_hi:[0,1]
	v_pk_mul_f32 v[28:29], v[42:43], v[26:27] op_sel_hi:[0,1]
	v_pk_mul_f32 v[38:39], v[42:43], v[38:39] op_sel_hi:[0,1]
	v_pk_mul_f32 v[30:31], v[42:43], v[40:41] op_sel_hi:[0,1]
	s_cbranch_vccnz .LBB0_446
	v_mul_f32_e32 v27, 0x3dd2d3e8, v28
	v_fmaak_f32 v27, v28, v27, 0x40135761
	v_mul_f32_e32 v37, 0x3dd2d3e8, v33
	v_mul_f32_e32 v40, 0x3dd2d3e8, v29
	v_mul_f32_e64 v27, v28, -v27
	v_fmaak_f32 v37, v33, v37, 0x40135761
	v_fmaak_f32 v40, v29, v40, 0x40135761
	v_exp_f32_e32 v27, v27
	v_mul_f32_e64 v37, v33, -v37
	v_mul_f32_e64 v40, v29, -v40
	v_exp_f32_e32 v37, v37
	v_exp_f32_e32 v41, v40
	v_add_f32_e32 v27, 1.0, v27
	v_rcp_f32_e32 v40, v27
	v_add_f32_e32 v27, 1.0, v37
	v_add_f32_e32 v37, 1.0, v41
	v_mul_f32_e32 v41, 0x3dd2d3e8, v38
	v_fmaak_f32 v41, v38, v41, 0x40135761
	v_mul_f32_e64 v41, v38, -v41
	v_exp_f32_e32 v42, v41
	v_mul_f32_e32 v41, 0x3dd2d3e8, v30
	v_fmaak_f32 v41, v30, v41, 0x40135761
	v_mul_f32_e64 v41, v30, -v41
	v_exp_f32_e32 v43, v41
	v_rcp_f32_e32 v41, v37
	v_add_f32_e32 v37, 1.0, v42
	v_rcp_f32_e32 v42, v37
	v_add_f32_e32 v37, 1.0, v43
	v_mul_f32_e32 v43, 0x3dd2d3e8, v39
	v_mul_f32_e32 v26, 0x3dd2d3e8, v32
	v_fmaak_f32 v43, v39, v43, 0x40135761
	v_mul_f32_e32 v44, 0x3dd2d3e8, v31
	v_fmaak_f32 v26, v32, v26, 0x40135761
	v_mul_f32_e64 v43, v39, -v43
	v_fmaak_f32 v44, v31, v44, 0x40135761
	v_mul_f32_e64 v26, v32, -v26
	v_exp_f32_e32 v43, v43
	v_mul_f32_e64 v44, v31, -v44
	v_exp_f32_e32 v26, v26
	v_exp_f32_e32 v45, v44
	v_rcp_f32_e32 v44, v37
	v_add_f32_e32 v37, 1.0, v43
	v_add_f32_e32 v26, 1.0, v26
	v_rcp_f32_e32 v43, v37
	v_add_f32_e32 v37, 1.0, v45
	v_rcp_f32_e32 v26, v26
	v_rcp_f32_e32 v27, v27
	v_rcp_f32_e32 v45, v37
	v_pk_mul_f32 v[38:39], v[38:39], v[42:43]
	v_pk_mul_f32 v[28:29], v[28:29], v[40:41]
	v_pk_mul_f32 v[32:33], v[32:33], v[26:27]
	v_pk_mul_f32 v[30:31], v[30:31], v[44:45]
.LBB0_446:
	v_mov_b64_e32 v[26:27], s[6:7]
	v_mad_i64_i32 v[26:27], s[28:29], v36, s57, v[26:27]
	v_lshl_add_u64 v[26:27], s[10:11], 1, v[26:27]
	v_lshl_add_u64 v[26:27], v[26:27], 0, s[20:21]
	v_lshl_add_u64 v[26:27], v[122:123], 1, v[26:27]
	v_cvt_pk_bf16_f32 v36, v32, v33
	v_cvt_pk_bf16_f32 v37, v38, v39
	v_cvt_pk_bf16_f32 v38, v28, v29
	v_cvt_pk_bf16_f32 v39, v30, v31
	global_store_dwordx4 v[26:27], v[36:39], off
	v_mov_b32_e32 v28, v190
	v_cvt_f32_i32_e32 v23, v23
	v_cvt_f32_i32_e32 v22, v22
	v_cvt_f32_i32_e32 v19, v19
	v_cvt_f32_i32_e32 v18, v18
	v_cvt_f32_i32_e32 v25, v25
	v_cvt_f32_i32_e32 v24, v24
	v_cvt_f32_i32_e32 v21, v21
	v_cvt_f32_i32_e32 v20, v20
	s_and_b64 vcc, exec, s[4:5]
	v_mul_f32_e32 v28, v141, v28
	v_pk_mul_f32 v[22:23], v[28:29], v[22:23] op_sel_hi:[0,1]
	v_pk_mul_f32 v[18:19], v[28:29], v[18:19] op_sel_hi:[0,1]
	v_pk_mul_f32 v[24:25], v[28:29], v[24:25] op_sel_hi:[0,1]
	v_pk_mul_f32 v[20:21], v[28:29], v[20:21] op_sel_hi:[0,1]
	s_cbranch_vccnz .LBB0_448
	v_mul_f32_e32 v30, 0x3dd2d3e8, v23
	v_fmaak_f32 v30, v23, v30, 0x40135761
	v_mul_f32_e32 v29, 0x3dd2d3e8, v18
	v_mul_f32_e64 v30, v23, -v30
	v_fmaak_f32 v29, v18, v29, 0x40135761
	v_exp_f32_e32 v31, v30
	v_mul_f32_e32 v30, 0x3dd2d3e8, v19
	v_mul_f32_e64 v29, v18, -v29
	v_fmaak_f32 v30, v19, v30, 0x40135761
	v_exp_f32_e32 v29, v29
	v_mul_f32_e64 v30, v19, -v30
	v_exp_f32_e32 v32, v30
	v_mul_f32_e32 v34, 0x3dd2d3e8, v25
	v_fmaak_f32 v34, v25, v34, 0x40135761
	v_add_f32_e32 v29, 1.0, v29
	v_mul_f32_e32 v33, 0x3dd2d3e8, v20
	v_mul_f32_e64 v34, v25, -v34
	v_mul_f32_e32 v28, 0x3dd2d3e8, v22
	v_rcp_f32_e32 v30, v29
	v_add_f32_e32 v29, 1.0, v31
	v_add_f32_e32 v31, 1.0, v32
	v_mul_f32_e32 v32, 0x3dd2d3e8, v24
	v_fmaak_f32 v33, v20, v33, 0x40135761
	v_exp_f32_e32 v35, v34
	v_mul_f32_e32 v34, 0x3dd2d3e8, v21
	v_fmaak_f32 v28, v22, v28, 0x40135761
	v_fmaak_f32 v32, v24, v32, 0x40135761
	v_mul_f32_e64 v33, v20, -v33
	v_fmaak_f32 v34, v21, v34, 0x40135761
	v_mul_f32_e64 v28, v22, -v28
	v_mul_f32_e64 v32, v24, -v32
	v_exp_f32_e32 v33, v33
	v_mul_f32_e64 v34, v21, -v34
	v_exp_f32_e32 v28, v28
	v_exp_f32_e32 v32, v32
	v_exp_f32_e32 v36, v34
	v_add_f32_e32 v33, 1.0, v33
	v_add_f32_e32 v28, 1.0, v28
	v_add_f32_e32 v32, 1.0, v32
	v_rcp_f32_e32 v34, v33
	v_add_f32_e32 v33, 1.0, v35
	v_add_f32_e32 v35, 1.0, v36
	v_rcp_f32_e32 v28, v28
	v_rcp_f32_e32 v29, v29
	v_rcp_f32_e32 v31, v31
	v_rcp_f32_e32 v32, v32
	v_rcp_f32_e32 v33, v33
	v_rcp_f32_e32 v35, v35
	v_pk_mul_f32 v[22:23], v[22:23], v[28:29]
	v_pk_mul_f32 v[18:19], v[18:19], v[30:31]
	v_pk_mul_f32 v[24:25], v[24:25], v[32:33]
	v_pk_mul_f32 v[20:21], v[20:21], v[34:35]
.LBB0_448:
	v_cvt_pk_bf16_f32 v22, v22, v23
	v_cvt_pk_bf16_f32 v23, v24, v25
	v_cvt_pk_bf16_f32 v25, v20, v21
	v_add_u32_e32 v20, 0xb0, v130
	v_cvt_pk_bf16_f32 v24, v18, v19
	v_ashrrev_i32_e32 v21, 31, v20
	global_store_dwordx4 v[26:27], v[22:25], off offset:256
	v_lshl_add_u64 v[18:19], v[20:21], 2, s[22:23]
	v_mov_b32_e32 v21, v191
	v_cvt_f32_i32_e32 v15, v15
	v_cvt_f32_i32_e32 v14, v14
	v_cvt_f32_i32_e32 v11, v11
	v_cvt_f32_i32_e32 v10, v10
	v_cvt_f32_i32_e32 v23, v17
	v_cvt_f32_i32_e32 v22, v16
	v_cvt_f32_i32_e32 v25, v13
	v_cvt_f32_i32_e32 v24, v12
	s_and_b64 vcc, exec, s[4:5]
	v_mul_f32_e32 v26, v141, v21
	v_pk_mul_f32 v[16:17], v[26:27], v[14:15] op_sel_hi:[0,1]
	v_pk_mul_f32 v[12:13], v[26:27], v[10:11] op_sel_hi:[0,1]
	v_pk_mul_f32 v[22:23], v[26:27], v[22:23] op_sel_hi:[0,1]
	v_pk_mul_f32 v[14:15], v[26:27], v[24:25] op_sel_hi:[0,1]
	s_cbranch_vccnz .LBB0_450
	v_mul_f32_e32 v11, 0x3dd2d3e8, v12
	v_fmaak_f32 v11, v12, v11, 0x40135761
	v_mul_f32_e32 v21, 0x3dd2d3e8, v17
	v_mul_f32_e32 v24, 0x3dd2d3e8, v13
	v_mul_f32_e64 v11, v12, -v11
	v_fmaak_f32 v21, v17, v21, 0x40135761
	v_fmaak_f32 v24, v13, v24, 0x40135761
	v_exp_f32_e32 v11, v11
	v_mul_f32_e64 v21, v17, -v21
	v_mul_f32_e64 v24, v13, -v24
	v_exp_f32_e32 v21, v21
	v_exp_f32_e32 v25, v24
	v_add_f32_e32 v11, 1.0, v11
	v_rcp_f32_e32 v24, v11
	v_add_f32_e32 v11, 1.0, v21
	v_add_f32_e32 v21, 1.0, v25
	v_mul_f32_e32 v25, 0x3dd2d3e8, v22
	v_fmaak_f32 v25, v22, v25, 0x40135761
	v_mul_f32_e64 v25, v22, -v25
	v_exp_f32_e32 v26, v25
	v_mul_f32_e32 v25, 0x3dd2d3e8, v14
	v_fmaak_f32 v25, v14, v25, 0x40135761
	v_mul_f32_e64 v25, v14, -v25
	v_exp_f32_e32 v27, v25
	v_rcp_f32_e32 v25, v21
	v_add_f32_e32 v21, 1.0, v26
	v_rcp_f32_e32 v26, v21
	v_add_f32_e32 v21, 1.0, v27
	v_mul_f32_e32 v27, 0x3dd2d3e8, v23
	v_mul_f32_e32 v10, 0x3dd2d3e8, v16
	v_fmaak_f32 v27, v23, v27, 0x40135761
	v_mul_f32_e32 v28, 0x3dd2d3e8, v15
	v_fmaak_f32 v10, v16, v10, 0x40135761
	v_mul_f32_e64 v27, v23, -v27
	v_fmaak_f32 v28, v15, v28, 0x40135761
	v_mul_f32_e64 v10, v16, -v10
	v_exp_f32_e32 v27, v27
	v_mul_f32_e64 v28, v15, -v28
	v_exp_f32_e32 v10, v10
	v_exp_f32_e32 v29, v28
	v_rcp_f32_e32 v28, v21
	v_add_f32_e32 v21, 1.0, v27
	v_add_f32_e32 v10, 1.0, v10
	v_rcp_f32_e32 v27, v21
	v_add_f32_e32 v21, 1.0, v29
	v_rcp_f32_e32 v10, v10
	v_rcp_f32_e32 v11, v11
	v_rcp_f32_e32 v29, v21
	v_pk_mul_f32 v[22:23], v[22:23], v[26:27]
	v_pk_mul_f32 v[12:13], v[12:13], v[24:25]
	v_pk_mul_f32 v[16:17], v[16:17], v[10:11]
	v_pk_mul_f32 v[14:15], v[14:15], v[28:29]
.LBB0_450:
	v_mov_b64_e32 v[10:11], s[6:7]
	v_mad_i64_i32 v[10:11], s[28:29], v20, s57, v[10:11]
	v_lshl_add_u64 v[10:11], s[10:11], 1, v[10:11]
	v_lshl_add_u64 v[10:11], v[10:11], 0, s[20:21]
	v_lshl_add_u64 v[10:11], v[122:123], 1, v[10:11]
	v_cvt_pk_bf16_f32 v20, v16, v17
	v_cvt_pk_bf16_f32 v21, v22, v23
	v_cvt_pk_bf16_f32 v22, v12, v13
	v_cvt_pk_bf16_f32 v23, v14, v15
	global_store_dwordx4 v[10:11], v[20:23], off
	v_mov_b32_e32 v12, v191
	v_cvt_f32_i32_e32 v7, v7
	v_cvt_f32_i32_e32 v6, v6
	v_cvt_f32_i32_e32 v3, v3
	v_cvt_f32_i32_e32 v2, v2
	v_cvt_f32_i32_e32 v9, v9
	v_cvt_f32_i32_e32 v8, v8
	v_cvt_f32_i32_e32 v5, v5
	v_cvt_f32_i32_e32 v4, v4
	s_and_b64 vcc, exec, s[4:5]
	v_mul_f32_e32 v12, v141, v12
	v_pk_mul_f32 v[6:7], v[12:13], v[6:7] op_sel_hi:[0,1]
	v_pk_mul_f32 v[2:3], v[12:13], v[2:3] op_sel_hi:[0,1]
	v_pk_mul_f32 v[8:9], v[12:13], v[8:9] op_sel_hi:[0,1]
	v_pk_mul_f32 v[4:5], v[12:13], v[4:5] op_sel_hi:[0,1]
	s_cbranch_vccnz .LBB0_452
	v_mul_f32_e32 v14, 0x3dd2d3e8, v7
	v_fmaak_f32 v14, v7, v14, 0x40135761
	v_mul_f32_e32 v13, 0x3dd2d3e8, v2
	v_mul_f32_e64 v14, v7, -v14
	v_fmaak_f32 v13, v2, v13, 0x40135761
	v_exp_f32_e32 v15, v14
	v_mul_f32_e32 v14, 0x3dd2d3e8, v3
	v_mul_f32_e64 v13, v2, -v13
	v_fmaak_f32 v14, v3, v14, 0x40135761
	v_exp_f32_e32 v13, v13
	v_mul_f32_e64 v14, v3, -v14
	v_exp_f32_e32 v16, v14
	v_mul_f32_e32 v18, 0x3dd2d3e8, v9
	v_fmaak_f32 v18, v9, v18, 0x40135761
	v_add_f32_e32 v13, 1.0, v13
	v_mul_f32_e32 v17, 0x3dd2d3e8, v4
	v_mul_f32_e64 v18, v9, -v18
	v_mul_f32_e32 v12, 0x3dd2d3e8, v6
	v_rcp_f32_e32 v14, v13
	v_add_f32_e32 v13, 1.0, v15
	v_add_f32_e32 v15, 1.0, v16
	v_mul_f32_e32 v16, 0x3dd2d3e8, v8
	v_fmaak_f32 v17, v4, v17, 0x40135761
	v_exp_f32_e32 v19, v18
	v_mul_f32_e32 v18, 0x3dd2d3e8, v5
	v_fmaak_f32 v12, v6, v12, 0x40135761
	v_fmaak_f32 v16, v8, v16, 0x40135761
	v_mul_f32_e64 v17, v4, -v17
	v_fmaak_f32 v18, v5, v18, 0x40135761
	v_mul_f32_e64 v12, v6, -v12
	v_mul_f32_e64 v16, v8, -v16
	v_exp_f32_e32 v17, v17
	v_mul_f32_e64 v18, v5, -v18
	v_exp_f32_e32 v12, v12
	v_exp_f32_e32 v16, v16
	v_exp_f32_e32 v20, v18
	v_add_f32_e32 v17, 1.0, v17
	v_add_f32_e32 v12, 1.0, v12
	v_add_f32_e32 v16, 1.0, v16
	v_rcp_f32_e32 v18, v17
	v_add_f32_e32 v17, 1.0, v19
	v_add_f32_e32 v19, 1.0, v20
	v_rcp_f32_e32 v12, v12
	v_rcp_f32_e32 v13, v13
	v_rcp_f32_e32 v15, v15
	v_rcp_f32_e32 v16, v16
	v_rcp_f32_e32 v17, v17
	v_rcp_f32_e32 v19, v19
	v_pk_mul_f32 v[6:7], v[6:7], v[12:13]
	v_pk_mul_f32 v[2:3], v[2:3], v[14:15]
	v_pk_mul_f32 v[8:9], v[8:9], v[16:17]
	v_pk_mul_f32 v[4:5], v[4:5], v[18:19]
